# v22 + packed f32 VALU (v_pk_mul/v_pk_fma) split into scalar pairs inside the two attention unit loops
# speedup vs baseline: 1.0057x; 1.0008x over previous
.LBB0_711:
	s_nop 10
	v_exp_f32_e32 v3, v98
	v_exp_f32_e32 v4, v82
	v_exp_f32_e32 v98, v112
	v_exp_f32_e32 v6, v99
	v_add_f32_e32 v3, 1.0, v3
	v_add_f32_e32 v5, 1.0, v4
	v_rcp_f32_e32 v4, v3
	v_exp_f32_e32 v3, v83
	v_exp_f32_e32 v99, v97
	v_exp_f32_e32 v16, v104
	v_exp_f32_e32 v82, v105
	v_add_f32_e32 v3, 1.0, v3
	v_rcp_f32_e32 v7, v3
	v_exp_f32_e32 v3, v84
	v_exp_f32_e32 v84, v106
	v_exp_f32_e32 v8, v100
	v_exp_f32_e32 v10, v101
	v_add_f32_e32 v3, 1.0, v3
	v_rcp_f32_e32 v9, v3
	v_exp_f32_e32 v3, v85
	v_exp_f32_e32 v14, v103
	v_exp_f32_e32 v12, v102
	v_add_f32_e32 v84, 1.0, v84
	v_add_f32_e32 v3, 1.0, v3
	v_rcp_f32_e32 v11, v3
	v_exp_f32_e32 v3, v86
	v_exp_f32_e32 v86, v107
	v_rcp_f32_e32 v84, v84
	v_add_f32_e32 v16, 1.0, v16
	v_add_f32_e32 v3, 1.0, v3
	v_rcp_f32_e32 v13, v3
	v_exp_f32_e32 v3, v87
	v_add_f32_e32 v86, 1.0, v86
	v_rcp_f32_e32 v86, v86
	v_add_f32_e32 v82, 1.0, v82
	v_add_f32_e32 v3, 1.0, v3
	v_rcp_f32_e32 v15, v3
	v_exp_f32_e32 v3, v88
	v_exp_f32_e32 v88, v108
	v_add_f32_e32 v8, 1.0, v8
	v_add_f32_e32 v10, 1.0, v10
	v_add_f32_e32 v3, 1.0, v3
	v_rcp_f32_e32 v17, v3
	v_exp_f32_e32 v3, v89
	v_add_f32_e32 v88, 1.0, v88
	v_rcp_f32_e32 v88, v88
	v_add_f32_e32 v14, 1.0, v14
	v_add_f32_e32 v3, 1.0, v3
	v_rcp_f32_e32 v83, v3
	v_exp_f32_e32 v3, v90
	v_exp_f32_e32 v90, v109
	v_rcp_f32_e32 v16, v16
	v_rcp_f32_e32 v82, v82
	v_add_f32_e32 v3, 1.0, v3
	v_rcp_f32_e32 v85, v3
	v_exp_f32_e32 v3, v91
	v_add_f32_e32 v90, 1.0, v90
	v_rcp_f32_e32 v90, v90
	v_add_f32_e32 v6, 1.0, v6
	v_add_f32_e32 v3, 1.0, v3
	v_rcp_f32_e32 v87, v3
	v_exp_f32_e32 v3, v92
	v_exp_f32_e32 v92, v110
	v_rcp_f32_e32 v8, v8
	v_rcp_f32_e32 v10, v10
	v_add_f32_e32 v3, 1.0, v3
	v_rcp_f32_e32 v89, v3
	v_exp_f32_e32 v3, v93
	v_add_f32_e32 v92, 1.0, v92
	v_rcp_f32_e32 v92, v92
	v_add_f32_e32 v12, 1.0, v12
	v_add_f32_e32 v3, 1.0, v3
	v_rcp_f32_e32 v91, v3
	v_exp_f32_e32 v3, v94
	v_exp_f32_e32 v94, v111
	v_rcp_f32_e32 v14, v14
	v_mul_f32_e32 v238, v88, v90
	v_mul_f32_e32 v239, v89, v91
	v_add_f32_e32 v3, 1.0, v3
	v_rcp_f32_e32 v93, v3
	v_exp_f32_e32 v3, v95
	v_add_f32_e32 v94, 1.0, v94
	v_rcp_f32_e32 v94, v94
	v_mul_f32_e32 v240, v86, v238
	v_mul_f32_e32 v241, v87, v239
	v_add_f32_e32 v3, 1.0, v3
	v_rcp_f32_e32 v95, v3
	v_exp_f32_e32 v3, v96
	v_add_f32_e32 v96, 1.0, v98
	v_exp_f32_e32 v98, v113
	v_rcp_f32_e32 v96, v96
	v_add_f32_e32 v3, 1.0, v3
	v_rcp_f32_e32 v97, v3
	v_add_f32_e32 v3, 1.0, v98
	v_rcp_f32_e32 v98, v3
	v_add_f32_e32 v3, 1.0, v99
	v_rcp_f32_e32 v99, v3
	v_rcp_f32_e32 v6, v6
	v_rcp_f32_e32 v12, v12
	v_mul_f32_e32 v242, v84, v240
	v_mul_f32_e32 v243, v85, v241
	v_mul_f32_e32 v248, v96, v98
	v_mul_f32_e32 v249, v97, v99
	v_rcp_f32_e32 v5, v5
	v_mul_f32_e32 v250, v94, v248
	v_mul_f32_e32 v251, v95, v249
	v_mov_b32_e32 v244, v242
	v_mul_f32_e32 v252, v92, v250
	v_mul_f32_e32 v253, v93, v251
	v_mul_f32_e32 v110, v16, v82
	v_mul_f32_e32 v111, v17, v83
	v_mov_b32_e32 v104, v252
	v_permlane32_swap_b32_e32 v242, v244
	s_nop 0
	v_permlane32_swap_b32_e32 v252, v104
	v_mul_f32_e32 v100, v8, v10
	v_mul_f32_e32 v101, v9, v11
	v_mul_f32_e32 v112, v14, v110
	v_mul_f32_e32 v113, v15, v111
	v_mul_f32_e32 v105, v191, v104
	v_mul_f32_e32 v245, v252, v104
	v_mov_b32_e32 v190, v242
	v_mul_f32_e32 v102, v6, v100
	v_mul_f32_e32 v103, v7, v101
	v_mul_f32_e32 v236, v12, v112
	v_mul_f32_e32 v237, v13, v113
	v_cndmask_b32_e64 v214, v191, v105, s[2:3]
	v_mul_f32_e32 v190, v190, v244
	v_mul_f32_e32 v191, v191, v245
	v_mul_f32_e32 v106, v4, v102
	v_mul_f32_e32 v107, v5, v103
	v_mov_b32_e32 v3, v236
	v_mul_f32_e32 v104, v191, v244
	v_mov_b32_e32 v206, v106
	v_permlane32_swap_b32_e32 v236, v3
	v_cndmask_b32_e64 v242, v191, v104, s[2:3]
	v_pk_mul_f32 v[190:191], v[190:191], v[190:191] op_sel:[0,1] op_sel_hi:[1,0]
	v_permlane32_swap_b32_e32 v106, v206
	v_mul_f32_e32 v104, v190, v3
	v_cndmask_b32_e64 v244, v190, v104, s[2:3]
	v_mul_f32_e32 v105, v236, v3
	v_mov_b32_e32 v104, v106
	v_mov_b32_e32 v207, v190
	v_mul_f32_e32 v104, v104, v206
	v_mul_f32_e32 v105, v105, v207
	v_mov_b32_e32 v246, v243
	v_mov_b32_e32 v247, v253
	v_mul_f32_e32 v3, v105, v206
	v_permlane32_swap_b32_e32 v243, v246
	v_permlane32_swap_b32_e32 v253, v247
	v_cndmask_b32_e64 v106, v105, v3, s[2:3]
	v_pk_mul_f32 v[104:105], v[104:105], v[104:105] op_sel:[0,1] op_sel_hi:[1,0]
	v_mul_f32_e32 v191, v253, v247
	v_mul_f32_e32 v3, v104, v247
	v_mov_b32_e32 v190, v243
	v_mov_b32_e32 v247, v104
	v_cndmask_b32_e64 v215, v104, v3, s[2:3]
	v_mul_f32_e32 v104, v190, v246
	v_mul_f32_e32 v105, v191, v247
	v_mov_b32_e32 v108, v107
	v_mov_b32_e32 v109, v237
	v_mul_f32_e32 v3, v105, v246
	v_permlane32_swap_b32_e32 v107, v108
	v_permlane32_swap_b32_e32 v237, v109
	v_cndmask_b32_e64 v243, v105, v3, s[2:3]
	v_pk_mul_f32 v[104:105], v[104:105], v[104:105] op_sel:[0,1] op_sel_hi:[1,0]
	v_mul_f32_e32 v191, v237, v109
	v_mul_f32_e32 v3, v104, v109
	v_mov_b32_e32 v190, v107
	v_mov_b32_e32 v109, v104
	v_cndmask_b32_e64 v245, v104, v3, s[2:3]
	v_mul_f32_e32 v104, v190, v108
	v_mul_f32_e32 v105, v191, v109
	s_nop 0
	v_mul_f32_e32 v3, v105, v108
	v_cndmask_b32_e64 v107, v105, v3, s[2:3]
	v_mul_f32_e32 v191, v104, v105
	v_mul_f32_e32 v104, v10, v106
	v_mul_f32_e32 v105, v11, v107
	v_mul_f32_e32 v100, v100, v106
	v_mul_f32_e32 v101, v101, v107
	v_mul_f32_e32 v102, v102, v106
	v_mul_f32_e32 v103, v103, v107
	v_fma_f32 v104, -v8, v104, v104
	v_fma_f32 v105, -v9, v105, v105
	v_fma_f32 v100, -v6, v100, v100
	v_fma_f32 v101, -v7, v101, v101
	v_mul_f32_e32 v6, v110, v244
	v_mul_f32_e32 v7, v111, v245
	v_mul_f32_e32 v8, v112, v244
	v_mul_f32_e32 v9, v113, v245
	v_fma_f32 v102, -v4, v102, v102
	v_fma_f32 v103, -v5, v103, v103
	v_mul_f32_e32 v4, v82, v244
	v_mul_f32_e32 v5, v83, v245
	v_fma_f32 v14, -v14, v6, v6
	v_fma_f32 v15, -v15, v7, v7
	v_fma_f32 v108, -v12, v8, v8
	v_fma_f32 v109, -v13, v9, v9
	v_mul_f32_e32 v6, v238, v242
	v_mul_f32_e32 v7, v239, v243
	v_mul_f32_e32 v8, v240, v242
	v_mul_f32_e32 v9, v241, v243
	v_fma_f32 v82, -v82, v244, v244
	v_fma_f32 v83, -v83, v245, v245
	v_fma_f32 v16, -v16, v4, v4
	v_fma_f32 v17, -v17, v5, v5
	v_mul_f32_e32 v4, v90, v242
	v_mul_f32_e32 v5, v91, v243
	v_fma_f32 v86, -v86, v6, v6
	v_fma_f32 v87, -v87, v7, v7
	v_fma_f32 v84, -v84, v8, v8
	v_fma_f32 v85, -v85, v9, v9
	v_mul_f32_e32 v6, v248, v214
	v_mul_f32_e32 v7, v249, v215
	v_mul_f32_e32 v8, v250, v214
	v_mul_f32_e32 v9, v251, v215
	v_fma_f32 v90, -v90, v242, v242
	v_fma_f32 v91, -v91, v243, v243
	v_fma_f32 v88, -v88, v4, v4
	v_fma_f32 v89, -v89, v5, v5
	v_fma_f32 v94, -v94, v6, v6
	v_fma_f32 v95, -v95, v7, v7
	v_fma_f32 v92, -v92, v8, v8
	v_fma_f32 v93, -v93, v9, v9
	v_cvt_pk_bf16_f32 v6, v109, v15
	v_cvt_pk_bf16_f32 v8, v85, v87
	v_cvt_pk_bf16_f32 v15, v16, v82
	v_cvt_pk_bf16_f32 v82, v84, v86
	ds_read_b64_tr_b16 v[86:87], v218 offset:0
	v_cvt_pk_bf16_f32 v7, v17, v83
	v_cvt_pk_bf16_f32 v9, v89, v91
	v_cvt_pk_bf16_f32 v83, v88, v90
	ds_read_b64_tr_b16 v[88:89], v218 offset:0x800
	ds_read_b64_tr_b16 v[90:91], v218 offset:0x1000
	v_fma_f32 v106, -v10, v106, v106
	v_fma_f32 v107, -v11, v107, v107
	v_mul_f32_e32 v4, v98, v214
	v_mul_f32_e32 v5, v99, v215
	v_cvt_pk_bf16_f32 v10, v93, v95
	v_cvt_pk_bf16_f32 v84, v92, v94
	ds_read_b64_tr_b16 v[92:93], v218 offset:0x1800
	v_fma_f32 v98, -v98, v214, v214
	v_fma_f32 v99, -v99, v215, v215
	v_fma_f32 v96, -v96, v4, v4
	v_fma_f32 v97, -v97, v5, v5
	ds_read_b64_tr_b16 v[94:95], v218 offset:0x2000
	v_cvt_pk_bf16_f32 v4, v103, v101
	v_cvt_pk_bf16_f32 v11, v97, v99
	v_cvt_pk_bf16_f32 v85, v96, v98
	ds_read_b64_tr_b16 v[96:97], v218 offset:0x2800
	ds_read_b64_tr_b16 v[98:99], v218 offset:0x3000
	v_cvt_pk_bf16_f32 v12, v102, v100
	ds_read_b64_tr_b16 v[100:101], v218 offset:0x3800
	s_waitcnt lgkmcnt(0)
	v_cvt_pk_bf16_f32 v5, v105, v107
	v_cvt_pk_bf16_f32 v13, v104, v106
	v_cvt_pk_bf16_f32 v14, v108, v14
	v_permlane32_swap_b32_e32 v4, v6
	v_permlane32_swap_b32_e32 v5, v7
	v_permlane32_swap_b32_e32 v8, v10
	v_permlane32_swap_b32_e32 v9, v11
	v_permlane32_swap_b32_e32 v12, v14
	v_permlane32_swap_b32_e32 v13, v15
	v_permlane32_swap_b32_e32 v82, v84
	v_permlane32_swap_b32_e32 v83, v85
	v_mfma_f32_32x32x16_bf16 v[66:81], v[4:7], v[86:89], v[66:81]
	ds_read_b64_tr_b16 v[86:87], v218 offset:0x200
	ds_read_b64_tr_b16 v[88:89], v218 offset:0xa00
	v_mfma_f32_32x32x16_bf16 v[66:81], v[8:11], v[90:93], v[66:81]
	ds_read_b64_tr_b16 v[90:91], v218 offset:0x1200
	ds_read_b64_tr_b16 v[92:93], v218 offset:0x1a00
	v_mfma_f32_32x32x16_bf16 v[66:81], v[12:15], v[94:97], v[66:81]
	ds_read_b64_tr_b16 v[94:95], v218 offset:0x2200
	ds_read_b64_tr_b16 v[96:97], v218 offset:0x2a00
	ds_read_b64_tr_b16 v[102:103], v218 offset:0x3200
	ds_read_b64_tr_b16 v[104:105], v218 offset:0x3a00
	s_waitcnt lgkmcnt(0)
	v_mfma_f32_32x32x16_bf16 v[66:81], v[82:85], v[98:101], v[66:81]
	v_mfma_f32_32x32x16_bf16 v[50:65], v[4:7], v[86:89], v[50:65]
	ds_read_b64_tr_b16 v[86:87], v218 offset:0x400
	ds_read_b64_tr_b16 v[88:89], v218 offset:0xc00
	v_mfma_f32_32x32x16_bf16 v[50:65], v[8:11], v[90:93], v[50:65]
	ds_read_b64_tr_b16 v[90:91], v218 offset:0x1400
	ds_read_b64_tr_b16 v[92:93], v218 offset:0x1c00
	v_mfma_f32_32x32x16_bf16 v[50:65], v[12:15], v[94:97], v[50:65]
	ds_read_b64_tr_b16 v[94:95], v218 offset:0x2400
	ds_read_b64_tr_b16 v[96:97], v218 offset:0x2c00
	ds_read_b64_tr_b16 v[98:99], v218 offset:0x3400
	ds_read_b64_tr_b16 v[100:101], v218 offset:0x3c00
	s_waitcnt lgkmcnt(0)
	v_mfma_f32_32x32x16_bf16 v[50:65], v[82:85], v[102:105], v[50:65]
	v_mfma_f32_32x32x16_bf16 v[34:49], v[4:7], v[86:89], v[34:49]
	ds_read_b64_tr_b16 v[86:87], v218 offset:0x600
	ds_read_b64_tr_b16 v[88:89], v218 offset:0xe00
	v_mfma_f32_32x32x16_bf16 v[34:49], v[8:11], v[90:93], v[34:49]
	ds_read_b64_tr_b16 v[90:91], v218 offset:0x1600
	ds_read_b64_tr_b16 v[92:93], v218 offset:0x1e00
	v_mfma_f32_32x32x16_bf16 v[34:49], v[12:15], v[94:97], v[34:49]
	ds_read_b64_tr_b16 v[94:95], v218 offset:0x2600
	ds_read_b64_tr_b16 v[96:97], v218 offset:0x2e00
	ds_read_b64_tr_b16 v[102:103], v218 offset:0x3600
	ds_read_b64_tr_b16 v[104:105], v218 offset:0x3e00
	s_waitcnt lgkmcnt(0)
	v_mfma_f32_32x32x16_bf16 v[34:49], v[82:85], v[98:101], v[34:49]
	v_mfma_f32_32x32x16_bf16 v[18:33], v[4:7], v[86:89], v[18:33]
	v_mfma_f32_32x32x16_bf16 v[18:33], v[8:11], v[90:93], v[18:33]
	v_mfma_f32_32x32x16_bf16 v[18:33], v[12:15], v[94:97], v[18:33]
	v_mfma_f32_32x32x16_bf16 v[18:33], v[82:85], v[102:105], v[18:33]

.LBB0_717:
	s_nop 10
	v_exp_f32_e32 v3, v98
	v_exp_f32_e32 v4, v82
	v_exp_f32_e32 v98, v112
	v_exp_f32_e32 v6, v99
	v_add_f32_e32 v3, 1.0, v3
	v_add_f32_e32 v5, 1.0, v4
	v_rcp_f32_e32 v4, v3
	v_exp_f32_e32 v3, v83
	v_exp_f32_e32 v99, v97
	v_exp_f32_e32 v16, v104
	v_exp_f32_e32 v82, v105
	v_add_f32_e32 v3, 1.0, v3
	v_rcp_f32_e32 v7, v3
	v_exp_f32_e32 v3, v84
	v_exp_f32_e32 v84, v106
	v_exp_f32_e32 v8, v100
	v_exp_f32_e32 v10, v101
	v_add_f32_e32 v3, 1.0, v3
	v_rcp_f32_e32 v9, v3
	v_exp_f32_e32 v3, v85
	v_exp_f32_e32 v14, v103
	v_exp_f32_e32 v12, v102
	v_add_f32_e32 v84, 1.0, v84
	v_add_f32_e32 v3, 1.0, v3
	v_rcp_f32_e32 v11, v3
	v_exp_f32_e32 v3, v86
	v_exp_f32_e32 v86, v107
	v_rcp_f32_e32 v84, v84
	v_add_f32_e32 v16, 1.0, v16
	v_add_f32_e32 v3, 1.0, v3
	v_rcp_f32_e32 v13, v3
	v_exp_f32_e32 v3, v87
	v_add_f32_e32 v86, 1.0, v86
	v_rcp_f32_e32 v86, v86
	v_add_f32_e32 v82, 1.0, v82
	v_add_f32_e32 v3, 1.0, v3
	v_rcp_f32_e32 v15, v3
	v_exp_f32_e32 v3, v88
	v_exp_f32_e32 v88, v108
	v_add_f32_e32 v8, 1.0, v8
	v_add_f32_e32 v10, 1.0, v10
	v_add_f32_e32 v3, 1.0, v3
	v_rcp_f32_e32 v17, v3
	v_exp_f32_e32 v3, v89
	v_add_f32_e32 v88, 1.0, v88
	v_rcp_f32_e32 v88, v88
	v_add_f32_e32 v14, 1.0, v14
	v_add_f32_e32 v3, 1.0, v3
	v_rcp_f32_e32 v83, v3
	v_exp_f32_e32 v3, v90
	v_exp_f32_e32 v90, v109
	v_rcp_f32_e32 v16, v16
	v_rcp_f32_e32 v82, v82
	v_add_f32_e32 v3, 1.0, v3
	v_rcp_f32_e32 v85, v3
	v_exp_f32_e32 v3, v91
	v_add_f32_e32 v90, 1.0, v90
	v_rcp_f32_e32 v90, v90
	v_add_f32_e32 v6, 1.0, v6
	v_add_f32_e32 v3, 1.0, v3
	v_rcp_f32_e32 v87, v3
	v_exp_f32_e32 v3, v92
	v_exp_f32_e32 v92, v110
	v_rcp_f32_e32 v8, v8
	v_rcp_f32_e32 v10, v10
	v_add_f32_e32 v3, 1.0, v3
	v_rcp_f32_e32 v89, v3
	v_exp_f32_e32 v3, v93
	v_add_f32_e32 v92, 1.0, v92
	v_rcp_f32_e32 v92, v92
	v_add_f32_e32 v12, 1.0, v12
	v_add_f32_e32 v3, 1.0, v3
	v_rcp_f32_e32 v91, v3
	v_exp_f32_e32 v3, v94
	v_exp_f32_e32 v94, v111
	v_rcp_f32_e32 v14, v14
	v_mul_f32_e32 v214, v88, v90
	v_mul_f32_e32 v215, v89, v91
	v_add_f32_e32 v3, 1.0, v3
	v_rcp_f32_e32 v93, v3
	v_exp_f32_e32 v3, v95
	v_add_f32_e32 v94, 1.0, v94
	v_rcp_f32_e32 v94, v94
	v_mul_f32_e32 v236, v86, v214
	v_mul_f32_e32 v237, v87, v215
	v_add_f32_e32 v3, 1.0, v3
	v_rcp_f32_e32 v95, v3
	v_exp_f32_e32 v3, v96
	v_add_f32_e32 v96, 1.0, v98
	v_exp_f32_e32 v98, v113
	v_rcp_f32_e32 v96, v96
	v_add_f32_e32 v3, 1.0, v3
	v_rcp_f32_e32 v97, v3
	v_add_f32_e32 v3, 1.0, v98
	v_rcp_f32_e32 v98, v3
	v_add_f32_e32 v3, 1.0, v99
	v_rcp_f32_e32 v99, v3
	v_rcp_f32_e32 v6, v6
	v_rcp_f32_e32 v12, v12
	v_mul_f32_e32 v238, v84, v236
	v_mul_f32_e32 v239, v85, v237
	v_mul_f32_e32 v244, v96, v98
	v_mul_f32_e32 v245, v97, v99
	v_rcp_f32_e32 v5, v5
	v_mul_f32_e32 v246, v94, v244
	v_mul_f32_e32 v247, v95, v245
	v_mov_b32_e32 v240, v238
	v_mul_f32_e32 v248, v92, v246
	v_mul_f32_e32 v249, v93, v247
	v_mul_f32_e32 v110, v16, v82
	v_mul_f32_e32 v111, v17, v83
	v_mov_b32_e32 v107, v248
	s_nop 1
	v_permlane32_swap_b32_e32 v248, v107
	v_permlane32_swap_b32_e32 v238, v240
	v_mul_f32_e32 v190, v191, v107
	v_mul_f32_e32 v100, v8, v10
	v_mul_f32_e32 v101, v9, v11
	v_mul_f32_e32 v112, v14, v110
	v_mul_f32_e32 v113, v15, v111
	v_cndmask_b32_e64 v250, v191, v190, s[2:3]
	v_mul_f32_e32 v241, v248, v107
	v_mov_b32_e32 v190, v238
	v_mul_f32_e32 v102, v6, v100
	v_mul_f32_e32 v103, v7, v101
	v_mul_f32_e32 v206, v12, v112
	v_mul_f32_e32 v207, v13, v113
	v_mul_f32_e32 v190, v190, v240
	v_mul_f32_e32 v191, v191, v241
	v_mul_f32_e32 v104, v4, v102
	v_mul_f32_e32 v105, v5, v103
	v_mov_b32_e32 v3, v206
	v_mul_f32_e32 v107, v191, v240
	v_mov_b32_e32 v106, v104
	v_permlane32_swap_b32_e32 v206, v3
	v_cndmask_b32_e64 v238, v191, v107, s[2:3]
	v_pk_mul_f32 v[190:191], v[190:191], v[190:191] op_sel:[0,1] op_sel_hi:[1,0]
	v_permlane32_swap_b32_e32 v104, v106
	v_mul_f32_e32 v107, v190, v3
	v_cndmask_b32_e64 v240, v190, v107, s[2:3]
	v_mul_f32_e32 v253, v206, v3
	v_mov_b32_e32 v252, v104
	v_mov_b32_e32 v107, v190
	v_mov_b32_e32 v242, v239
	v_mov_b32_e32 v243, v249
	v_mul_f32_e32 v190, v252, v106
	v_mul_f32_e32 v191, v253, v107
	v_permlane32_swap_b32_e32 v239, v242
	v_permlane32_swap_b32_e32 v249, v243
	v_mul_f32_e32 v3, v191, v106
	v_mul_f32_e32 v106, v190, v191
	v_mul_f32_e32 v107, v191, v190
	v_cndmask_b32_e64 v104, v191, v3, s[2:3]
	v_mul_f32_e32 v3, v106, v243
	v_mul_f32_e32 v191, v249, v243
	v_mov_b32_e32 v190, v239
	v_mov_b32_e32 v243, v106
	v_cndmask_b32_e64 v251, v106, v3, s[2:3]
	v_mul_f32_e32 v106, v190, v242
	v_mul_f32_e32 v107, v191, v243
	v_mov_b32_e32 v108, v105
	v_mov_b32_e32 v109, v207
	v_mul_f32_e32 v3, v107, v242
	v_permlane32_swap_b32_e32 v105, v108
	v_permlane32_swap_b32_e32 v207, v109
	v_cndmask_b32_e64 v239, v107, v3, s[2:3]
	v_pk_mul_f32 v[106:107], v[106:107], v[106:107] op_sel:[0,1] op_sel_hi:[1,0]
	v_mul_f32_e32 v191, v207, v109
	v_mul_f32_e32 v3, v106, v109
	v_mov_b32_e32 v190, v105
	v_mov_b32_e32 v109, v106
	v_cndmask_b32_e64 v241, v106, v3, s[2:3]
	v_mul_f32_e32 v106, v190, v108
	v_mul_f32_e32 v107, v191, v109
	s_nop 0
	v_mul_f32_e32 v3, v107, v108
	v_cndmask_b32_e64 v105, v107, v3, s[2:3]
	v_mul_f32_e32 v191, v106, v107
	v_mul_f32_e32 v106, v10, v104
	v_mul_f32_e32 v107, v11, v105
	v_mul_f32_e32 v100, v100, v104
	v_mul_f32_e32 v101, v101, v105
	v_mul_f32_e32 v102, v102, v104
	v_mul_f32_e32 v103, v103, v105
	v_fma_f32 v106, -v8, v106, v106
	v_fma_f32 v107, -v9, v107, v107
	v_fma_f32 v100, -v6, v100, v100
	v_fma_f32 v101, -v7, v101, v101
	v_mul_f32_e32 v6, v110, v240
	v_mul_f32_e32 v7, v111, v241
	v_mul_f32_e32 v8, v112, v240
	v_mul_f32_e32 v9, v113, v241
	v_fma_f32 v102, -v4, v102, v102
	v_fma_f32 v103, -v5, v103, v103
	v_mul_f32_e32 v4, v82, v240
	v_mul_f32_e32 v5, v83, v241
	v_fma_f32 v14, -v14, v6, v6
	v_fma_f32 v15, -v15, v7, v7
	v_fma_f32 v108, -v12, v8, v8
	v_fma_f32 v109, -v13, v9, v9
	v_mul_f32_e32 v6, v214, v238
	v_mul_f32_e32 v7, v215, v239
	v_mul_f32_e32 v8, v236, v238
	v_mul_f32_e32 v9, v237, v239
	v_fma_f32 v82, -v82, v240, v240
	v_fma_f32 v83, -v83, v241, v241
	v_fma_f32 v16, -v16, v4, v4
	v_fma_f32 v17, -v17, v5, v5
	v_mul_f32_e32 v4, v90, v238
	v_mul_f32_e32 v5, v91, v239
	v_fma_f32 v86, -v86, v6, v6
	v_fma_f32 v87, -v87, v7, v7
	v_fma_f32 v84, -v84, v8, v8
	v_fma_f32 v85, -v85, v9, v9
	v_mul_f32_e32 v6, v244, v250
	v_mul_f32_e32 v7, v245, v251
	v_mul_f32_e32 v8, v246, v250
	v_mul_f32_e32 v9, v247, v251
	v_fma_f32 v90, -v90, v238, v238
	v_fma_f32 v91, -v91, v239, v239
	v_fma_f32 v88, -v88, v4, v4
	v_fma_f32 v89, -v89, v5, v5
	v_fma_f32 v94, -v94, v6, v6
	v_fma_f32 v95, -v95, v7, v7
	v_fma_f32 v92, -v92, v8, v8
	v_fma_f32 v93, -v93, v9, v9
	v_cvt_pk_bf16_f32 v6, v109, v15
	v_cvt_pk_bf16_f32 v8, v85, v87
	v_cvt_pk_bf16_f32 v15, v16, v82
	v_cvt_pk_bf16_f32 v82, v84, v86
	ds_read_b64_tr_b16 v[86:87], v228 offset:0
	v_cvt_pk_bf16_f32 v7, v17, v83
	v_cvt_pk_bf16_f32 v9, v89, v91
	v_cvt_pk_bf16_f32 v83, v88, v90
	ds_read_b64_tr_b16 v[88:89], v228 offset:0x800
	ds_read_b64_tr_b16 v[90:91], v228 offset:0x1000
	v_fma_f32 v104, -v10, v104, v104
	v_fma_f32 v105, -v11, v105, v105
	v_mul_f32_e32 v4, v98, v250
	v_mul_f32_e32 v5, v99, v251
	v_cvt_pk_bf16_f32 v10, v93, v95
	v_cvt_pk_bf16_f32 v84, v92, v94
	ds_read_b64_tr_b16 v[92:93], v228 offset:0x1800
	v_fma_f32 v98, -v98, v250, v250
	v_fma_f32 v99, -v99, v251, v251
	v_fma_f32 v96, -v96, v4, v4
	v_fma_f32 v97, -v97, v5, v5
	ds_read_b64_tr_b16 v[94:95], v228 offset:0x2000
	v_cvt_pk_bf16_f32 v4, v103, v101
	v_cvt_pk_bf16_f32 v11, v97, v99
	v_cvt_pk_bf16_f32 v85, v96, v98
	ds_read_b64_tr_b16 v[96:97], v228 offset:0x2800
	ds_read_b64_tr_b16 v[98:99], v228 offset:0x3000
	v_cvt_pk_bf16_f32 v12, v102, v100
	ds_read_b64_tr_b16 v[100:101], v228 offset:0x3800
	s_waitcnt lgkmcnt(0)
	v_cvt_pk_bf16_f32 v5, v107, v105
	v_cvt_pk_bf16_f32 v13, v106, v104
	v_cvt_pk_bf16_f32 v14, v108, v14
	v_permlane32_swap_b32_e32 v4, v6
	v_permlane32_swap_b32_e32 v5, v7
	v_permlane32_swap_b32_e32 v8, v10
	v_permlane32_swap_b32_e32 v9, v11
	v_permlane32_swap_b32_e32 v12, v14
	v_permlane32_swap_b32_e32 v13, v15
	v_permlane32_swap_b32_e32 v82, v84
	v_permlane32_swap_b32_e32 v83, v85
	v_mfma_f32_32x32x16_bf16 v[66:81], v[4:7], v[86:89], v[66:81]
	ds_read_b64_tr_b16 v[86:87], v228 offset:0x200
	ds_read_b64_tr_b16 v[88:89], v228 offset:0xa00
	v_mfma_f32_32x32x16_bf16 v[66:81], v[8:11], v[90:93], v[66:81]
	ds_read_b64_tr_b16 v[90:91], v228 offset:0x1200
	ds_read_b64_tr_b16 v[92:93], v228 offset:0x1a00
	v_mfma_f32_32x32x16_bf16 v[66:81], v[12:15], v[94:97], v[66:81]
	ds_read_b64_tr_b16 v[94:95], v228 offset:0x2200
	ds_read_b64_tr_b16 v[96:97], v228 offset:0x2a00
	ds_read_b64_tr_b16 v[102:103], v228 offset:0x3200
	ds_read_b64_tr_b16 v[104:105], v228 offset:0x3a00
	s_waitcnt lgkmcnt(0)
	v_mfma_f32_32x32x16_bf16 v[66:81], v[82:85], v[98:101], v[66:81]
	v_mfma_f32_32x32x16_bf16 v[50:65], v[4:7], v[86:89], v[50:65]
	ds_read_b64_tr_b16 v[86:87], v228 offset:0x400
	ds_read_b64_tr_b16 v[88:89], v228 offset:0xc00
	v_mfma_f32_32x32x16_bf16 v[50:65], v[8:11], v[90:93], v[50:65]
	ds_read_b64_tr_b16 v[90:91], v228 offset:0x1400
	ds_read_b64_tr_b16 v[92:93], v228 offset:0x1c00
	v_mfma_f32_32x32x16_bf16 v[50:65], v[12:15], v[94:97], v[50:65]
	ds_read_b64_tr_b16 v[94:95], v228 offset:0x2400
	ds_read_b64_tr_b16 v[96:97], v228 offset:0x2c00
	ds_read_b64_tr_b16 v[98:99], v228 offset:0x3400
	ds_read_b64_tr_b16 v[100:101], v228 offset:0x3c00
	s_waitcnt lgkmcnt(0)
	v_mfma_f32_32x32x16_bf16 v[50:65], v[82:85], v[102:105], v[50:65]
	v_mfma_f32_32x32x16_bf16 v[34:49], v[4:7], v[86:89], v[34:49]
	ds_read_b64_tr_b16 v[86:87], v228 offset:0x600
	ds_read_b64_tr_b16 v[88:89], v228 offset:0xe00
	v_mfma_f32_32x32x16_bf16 v[34:49], v[8:11], v[90:93], v[34:49]
	ds_read_b64_tr_b16 v[90:91], v228 offset:0x1600
	ds_read_b64_tr_b16 v[92:93], v228 offset:0x1e00
	v_mfma_f32_32x32x16_bf16 v[34:49], v[12:15], v[94:97], v[34:49]
	ds_read_b64_tr_b16 v[94:95], v228 offset:0x2600
	ds_read_b64_tr_b16 v[96:97], v228 offset:0x2e00
	ds_read_b64_tr_b16 v[102:103], v228 offset:0x3600
	ds_read_b64_tr_b16 v[104:105], v228 offset:0x3e00
	s_waitcnt lgkmcnt(0)
	v_mfma_f32_32x32x16_bf16 v[34:49], v[82:85], v[98:101], v[34:49]
	v_mfma_f32_32x32x16_bf16 v[18:33], v[4:7], v[86:89], v[18:33]
	v_mfma_f32_32x32x16_bf16 v[18:33], v[8:11], v[90:93], v[18:33]
	v_mfma_f32_32x32x16_bf16 v[18:33], v[12:15], v[94:97], v[18:33]
	v_mfma_f32_32x32x16_bf16 v[18:33], v[82:85], v[102:105], v[18:33]
